# baseline (speedup 1.0000x reference)
.LBB1_35:
	s_barrier
	s_xor_b64 s[8:9], s[10:11], -1
	s_andn2_b64 vcc, exec, s[8:9]
	s_cbranch_vccnz .LBB1_44
	s_mov_b64 s[52:53], s[6:7]
	s_mov_b32 s45, 0
	s_branch .LBB1_38
